# up-weight fp8 conversion stores (barrier waits + flush, and the P0 fp8 copies) with default cache policy instead of nt
# baseline (speedup 1.0000x reference)
; __device__ __forceinline__ int lane_id_now() { unsigned z = 0u; asm volatile("" : "+v"(z)); return (int)__builtin_amdgcn_mbcnt_hi(~0u, __builtin_amdgcn_mbcnt_lo(~0u, z)); }
; #define GAS __attribute__((address_space(1)))
; template <bool GAIN, bool NT = false> __device__ __forceinline__ void titem8_load(const TItem& d, int lane, f32x4 (&r)[16], f32x4 (&g)[4]) {
;     const int q = lane & 7, kg = lane >> 3; const unsigned lo = (unsigned)((16 * kg) * d.N + 4 * q) * 4u;
;     const GAS char* base = (const GAS char*)d.src;
; #pragma unroll
;     for (int j = 0; j < 16; ++j) { const GAS f32x4* p = (const GAS f32x4*)(base + (size_t)j * (size_t)d.N * 4 + lo); r[j] = NT ? __builtin_nontemporal_load(p) : *p; }
;     if constexpr (GAIN) { const GAS char* gb = (const GAS char*)d.gain; const unsigned go = (unsigned)(16 * kg) * 4u;
; #pragma unroll
;         for (int j4 = 0; j4 < 4; ++j4) g[j4] = *(const GAS f32x4*)(gb + 16 * j4 + go); }
;     asm volatile("" ::: "memory"); __builtin_amdgcn_sched_barrier(0);
; }
; __device__ __forceinline__ bool cv_one(const CvWork& w) {
;     ...
;     TItem d; { int r = it; const int e = r / CV_I_UP; r -= e * CV_I_UP; const int nb_ = 2 * FF / 32, kb = r / nb_, nbi = r % nb_;
;         d.src = w.wup + (size_t)e * D * 2 * FF + (size_t)(128 * kb) * (2 * FF) + 32 * nbi; d.dst = (bf16*)(w.wup8 + (size_t)e * 2 * FF * D + (size_t)(32 * nbi) * D + 128 * kb);
;         d.gain = w.gain + 128 * kb; d.N = 2 * FF; d.ldk = D; }
;     const int lane = lane_id_now();
;     f32x4 r[16], g[4]; titem8_load<true, true>(d, lane, r, g); titem8_store<true, true>(d, lane, r, g);
.LBB0_212:
	s_and_b64 vcc, exec, s[6:7]
	s_cbranch_vccz .LBB0_214
	s_ashr_i32 s4, s29, 31
	s_lshr_b32 s4, s4, 21
	s_add_i32 s5, s29, s4
	s_ashr_i32 s4, s5, 11
	s_and_b32 s5, s5, 0xfffff800
	s_sub_i32 s5, s29, s5
	s_ashr_i32 s6, s5, 31
	s_lshr_b32 s6, s6, 25
	s_add_i32 s6, s5, s6
	s_and_b32 s6, s6, 0xffffff80
	s_sub_i32 s30, s5, s6
	s_ashr_i32 s5, s4, 31
	s_lshl_b64 s[8:9], s[4:5], 25
	s_add_u32 s31, s58, s8
	s_addc_u32 s33, s59, s9
	s_ashr_i32 s7, s6, 31
	v_mov_b32_e32 v0, 0
	s_lshl_b64 s[8:9], s[6:7], 14
	s_add_u32 s34, s31, s8
	v_mbcnt_lo_u32_b32 v0, -1, v0
	s_addc_u32 s33, s33, s9
	s_lshl_b32 s8, s30, 5
	v_mbcnt_hi_u32_b32 v0, -1, v0
	s_ashr_i32 s9, s8, 31
	v_lshlrev_b32_e32 v7, 1, v0
	v_lshlrev_b32_e32 v0, 2, v0
	s_lshl_b64 s[30:31], s[8:9], 2
	v_and_b32_e32 v88, 28, v0
	s_add_u32 s30, s34, s30
	v_and_b32_e32 v7, -16, v7
	v_lshlrev_b32_e32 v0, 2, v88
	s_addc_u32 s31, s33, s31
	v_lshl_or_b32 v0, v7, 14, v0
	v_lshl_add_u64 v[68:69], s[30:31], 0, v[0:1]
	s_waitcnt vmcnt(13)
	v_add_co_u32_e32 v12, vcc, s11, v68
	s_lshl_b64 s[4:5], s[4:5], 23
	s_nop 0
	v_addc_co_u32_e32 v13, vcc, 0, v69, vcc
	s_waitcnt vmcnt(12)
	v_add_co_u32_e32 v16, vcc, s12, v68
	s_add_u32 s33, s88, s4
	s_nop 0
	v_addc_co_u32_e32 v17, vcc, 0, v69, vcc
	s_waitcnt vmcnt(11)
	v_add_co_u32_e32 v20, vcc, s13, v68
	s_addc_u32 s34, s87, s5
	s_nop 0
	v_addc_co_u32_e32 v21, vcc, 0, v69, vcc
	s_waitcnt vmcnt(10)
	v_add_co_u32_e32 v24, vcc, s3, v68
	s_lshl_b64 s[4:5], s[8:9], 11
	s_nop 0
	v_addc_co_u32_e32 v25, vcc, 0, v69, vcc
	s_waitcnt vmcnt(9)
	v_add_co_u32_e32 v28, vcc, s14, v68
	s_add_u32 s4, s33, s4
	s_nop 0
	v_addc_co_u32_e32 v29, vcc, 0, v69, vcc
	s_waitcnt vmcnt(8)
	v_add_co_u32_e32 v32, vcc, s15, v68
	s_addc_u32 s5, s34, s5
	s_nop 0
	v_addc_co_u32_e32 v33, vcc, 0, v69, vcc
	s_waitcnt vmcnt(7)
	v_add_co_u32_e32 v36, vcc, s16, v68
	s_add_u32 s4, s4, s6
	s_nop 0
	v_addc_co_u32_e32 v37, vcc, 0, v69, vcc
	s_waitcnt vmcnt(6)
	v_add_co_u32_e32 v40, vcc, s17, v68
	s_addc_u32 s5, s5, s7
	s_nop 0
	v_addc_co_u32_e32 v41, vcc, 0, v69, vcc
	s_waitcnt vmcnt(5)
	v_add_co_u32_e32 v44, vcc, s18, v68
	s_lshl_b64 s[6:7], s[6:7], 2
	s_nop 0
	v_addc_co_u32_e32 v45, vcc, 0, v69, vcc
	s_waitcnt vmcnt(4)
	v_add_co_u32_e32 v48, vcc, s19, v68
	s_add_u32 s6, s52, s6
	s_nop 0
	v_addc_co_u32_e32 v49, vcc, 0, v69, vcc
	s_waitcnt vmcnt(3)
	v_add_co_u32_e32 v52, vcc, s20, v68
	s_addc_u32 s7, s53, s7
	s_nop 0
	v_addc_co_u32_e32 v53, vcc, 0, v69, vcc
	s_waitcnt vmcnt(2)
	v_add_co_u32_e32 v56, vcc, s21, v68
	global_load_dwordx4 v[8:11], v0, s[30:31] nt
	s_nop 0
	v_addc_co_u32_e32 v57, vcc, 0, v69, vcc
	s_waitcnt vmcnt(2)
	v_add_co_u32_e32 v60, vcc, s22, v68
	v_lshlrev_b32_e32 v0, 2, v7
	s_nop 0
	v_addc_co_u32_e32 v61, vcc, 0, v69, vcc
	v_add_co_u32_e32 v64, vcc, s23, v68
	global_load_dwordx4 v[12:15], v[12:13], off nt
	s_nop 0
	global_load_dwordx4 v[16:19], v[16:17], off nt
	v_addc_co_u32_e32 v65, vcc, 0, v69, vcc
	v_add_co_u32_e32 v68, vcc, s24, v68
	global_load_dwordx4 v[20:23], v[20:21], off nt
	s_nop 0
	global_load_dwordx4 v[24:27], v[24:25], off nt
	v_addc_co_u32_e32 v69, vcc, 0, v69, vcc
	global_load_dwordx4 v[28:31], v[28:29], off nt
	s_nop 0
	global_load_dwordx4 v[32:35], v[32:33], off nt
	s_nop 0
	global_load_dwordx4 v[36:39], v[36:37], off nt
	s_nop 0
	global_load_dwordx4 v[40:43], v[40:41], off nt
	s_nop 0
	global_load_dwordx4 v[44:47], v[44:45], off nt
	s_nop 0
	global_load_dwordx4 v[48:51], v[48:49], off nt
	s_nop 0
	global_load_dwordx4 v[52:55], v[52:53], off nt
	s_nop 0
	global_load_dwordx4 v[56:59], v[56:57], off nt
	s_nop 0
	global_load_dwordx4 v[60:63], v[60:61], off nt
	s_nop 0
	global_load_dwordx4 v[64:67], v[64:65], off nt
	s_nop 0
	global_load_dwordx4 v[68:71], v[68:69], off nt
	s_nop 0
	global_load_dwordx4 v[72:75], v0, s[6:7] offset:48
	global_load_dwordx4 v[76:79], v0, s[6:7] offset:32
	global_load_dwordx4 v[80:83], v0, s[6:7] offset:16
	global_load_dwordx4 v[84:87], v0, s[6:7]
	s_waitcnt vmcnt(0)
; #define GAS __attribute__((address_space(1)))
; template <bool GAIN, bool NT = false> __device__ __forceinline__ void titem8_store(const TItem& d, int lane, const f32x4 (&r)[16], const f32x4 (&g)[4]) {
;     const int q = lane & 7, kg = lane >> 3; const unsigned lo = (unsigned)((4 * q) * d.ldk + 16 * kg);
;     GAS char* base = (GAS char*)d.dst;
;     f32x4 s[16];
; #pragma unroll
;     for (int j = 0; j < 16; ++j) s[j] = r[j] * ((GAIN ? g[j >> 2][j & 3] : 1.0f) * W8_SCALE);
; #pragma unroll
;     for (int i = 0; i < 4; ++i) { v4u w;
;         w.x = pk4_fp8w(s[0][i], s[1][i], s[2][i], s[3][i]); w.y = pk4_fp8w(s[4][i], s[5][i], s[6][i], s[7][i]);
;         w.z = pk4_fp8w(s[8][i], s[9][i], s[10][i], s[11][i]); w.w = pk4_fp8w(s[12][i], s[13][i], s[14][i], s[15][i]);
;         GAS v4u* p = (GAS v4u*)(base + (size_t)i * (size_t)d.ldk + lo);
;         if (NT) __builtin_nontemporal_store(w, p); else *p = w; }
; }
; __device__ __forceinline__ bool cv_one(const CvWork& w) {
;     ...
;     f32x4 r[16], g[4]; titem8_load<true, true>(d, lane, r, g); titem8_store<true, true>(d, lane, r, g);
;     w.cur[2 * w.wave] = it + 1;
	v_mul_f32_e32 v84, 0x43800000, v84
	v_pk_mul_f32 v[90:91], v[8:9], v[84:85] op_sel_hi:[1,0]
	v_mul_f32_e32 v8, 0x43800000, v85
	v_lshl_add_u32 v0, v88, 11, v7
	v_pk_mul_f32 v[88:89], v[10:11], v[84:85] op_sel_hi:[1,0]
	v_pk_mul_f32 v[84:85], v[14:15], v[8:9] op_sel_hi:[1,0]
	v_pk_mul_f32 v[12:13], v[12:13], v[8:9] op_sel_hi:[1,0]
	v_mul_f32_e32 v8, 0x43800000, v86
	v_pk_mul_f32 v[18:19], v[18:19], v[8:9] op_sel_hi:[1,0]
	v_pk_mul_f32 v[14:15], v[16:17], v[8:9] op_sel_hi:[1,0]
	v_mul_f32_e32 v8, 0x43800000, v87
	v_pk_mul_f32 v[16:17], v[22:23], v[8:9] op_sel_hi:[1,0]
	v_pk_mul_f32 v[20:21], v[20:21], v[8:9] op_sel_hi:[1,0]
	v_mul_f32_e32 v8, 0x43800000, v80
	v_pk_mul_f32 v[22:23], v[26:27], v[8:9] op_sel_hi:[1,0]
	v_pk_mul_f32 v[24:25], v[24:25], v[8:9] op_sel_hi:[1,0]
	v_mul_f32_e32 v8, 0x43800000, v81
	v_pk_mul_f32 v[26:27], v[30:31], v[8:9] op_sel_hi:[1,0]
	v_pk_mul_f32 v[28:29], v[28:29], v[8:9] op_sel_hi:[1,0]
	v_mul_f32_e32 v8, 0x43800000, v82
	v_pk_mul_f32 v[30:31], v[34:35], v[8:9] op_sel_hi:[1,0]
	v_pk_mul_f32 v[32:33], v[32:33], v[8:9] op_sel_hi:[1,0]
	v_mul_f32_e32 v8, 0x43800000, v83
	v_pk_mul_f32 v[34:35], v[38:39], v[8:9] op_sel_hi:[1,0]
	v_pk_mul_f32 v[36:37], v[36:37], v[8:9] op_sel_hi:[1,0]
	v_mul_f32_e32 v8, 0x43800000, v76
	v_pk_mul_f32 v[38:39], v[42:43], v[8:9] op_sel_hi:[1,0]
	v_pk_mul_f32 v[40:41], v[40:41], v[8:9] op_sel_hi:[1,0]
	v_mul_f32_e32 v8, 0x43800000, v77
	v_pk_mul_f32 v[42:43], v[46:47], v[8:9] op_sel_hi:[1,0]
	v_pk_mul_f32 v[44:45], v[44:45], v[8:9] op_sel_hi:[1,0]
	v_mul_f32_e32 v8, 0x43800000, v78
	v_pk_mul_f32 v[46:47], v[50:51], v[8:9] op_sel_hi:[1,0]
	v_pk_mul_f32 v[48:49], v[48:49], v[8:9] op_sel_hi:[1,0]
	v_mul_f32_e32 v8, 0x43800000, v79
	v_pk_mul_f32 v[50:51], v[54:55], v[8:9] op_sel_hi:[1,0]
	v_pk_mul_f32 v[52:53], v[52:53], v[8:9] op_sel_hi:[1,0]
	v_mul_f32_e32 v8, 0x43800000, v72
	v_pk_mul_f32 v[54:55], v[58:59], v[8:9] op_sel_hi:[1,0]
	v_pk_mul_f32 v[56:57], v[56:57], v[8:9] op_sel_hi:[1,0]
	v_mul_f32_e32 v8, 0x43800000, v73
	v_pk_mul_f32 v[58:59], v[62:63], v[8:9] op_sel_hi:[1,0]
	v_pk_mul_f32 v[60:61], v[60:61], v[8:9] op_sel_hi:[1,0]
	v_mul_f32_e32 v8, 0x43800000, v74
	v_pk_mul_f32 v[62:63], v[66:67], v[8:9] op_sel_hi:[1,0]
	v_pk_mul_f32 v[64:65], v[64:65], v[8:9] op_sel_hi:[1,0]
	v_med3_f32 v7, v90, s25, v6
	v_med3_f32 v9, v12, s25, v6
	v_mov_b32_e32 v8, v1
	v_cvt_pk_fp8_f32 v8, v7, v9
	v_med3_f32 v11, v24, s25, v6
	v_med3_f32 v12, v28, s25, v6
	v_mov_b32_e32 v9, v1
	v_cvt_pk_fp8_f32 v9, v11, v12
	v_med3_f32 v7, v14, s25, v6
	v_med3_f32 v10, v20, s25, v6
	v_cvt_pk_fp8_f32 v8, v7, v10 op_sel:[0,0,1]
	v_med3_f32 v7, v32, s25, v6
	v_med3_f32 v10, v36, s25, v6
	v_cvt_pk_fp8_f32 v9, v7, v10 op_sel:[0,0,1]
	v_med3_f32 v7, v40, s25, v6
	v_med3_f32 v11, v44, s25, v6
	v_mov_b32_e32 v10, v1
	v_cvt_pk_fp8_f32 v10, v7, v11
	v_med3_f32 v14, v56, s25, v6
	v_med3_f32 v20, v60, s25, v6
	v_mov_b32_e32 v11, v1
	v_cvt_pk_fp8_f32 v11, v14, v20
	v_mul_f32_e32 v66, 0x43800000, v75
	v_pk_mul_f32 v[68:69], v[68:69], v[66:67] op_sel_hi:[1,0]
	v_med3_f32 v7, v48, s25, v6
	v_med3_f32 v12, v52, s25, v6
	v_cvt_pk_fp8_f32 v10, v7, v12 op_sel:[0,0,1]
	v_med3_f32 v7, v64, s25, v6
	v_med3_f32 v12, v68, s25, v6
	v_cvt_pk_fp8_f32 v11, v7, v12 op_sel:[0,0,1]
	v_med3_f32 v7, v91, s25, v6
	v_med3_f32 v13, v13, s25, v6
	v_mov_b32_e32 v12, v1
	v_cvt_pk_fp8_f32 v12, v7, v13
	v_med3_f32 v7, v15, s25, v6
	v_med3_f32 v15, v25, s25, v6
	v_med3_f32 v20, v29, s25, v6
	v_mov_b32_e32 v13, v1
	v_cvt_pk_fp8_f32 v13, v15, v20
	v_med3_f32 v14, v21, s25, v6
	v_cvt_pk_fp8_f32 v12, v7, v14 op_sel:[0,0,1]
	v_med3_f32 v7, v33, s25, v6
	v_med3_f32 v14, v37, s25, v6
	v_cvt_pk_fp8_f32 v13, v7, v14 op_sel:[0,0,1]
	v_med3_f32 v7, v41, s25, v6
	v_med3_f32 v15, v45, s25, v6
	v_mov_b32_e32 v14, v1
	v_cvt_pk_fp8_f32 v14, v7, v15
	v_med3_f32 v21, v57, s25, v6
	v_med3_f32 v24, v61, s25, v6
	v_mov_b32_e32 v15, v1
	v_cvt_pk_fp8_f32 v15, v21, v24
	v_med3_f32 v7, v49, s25, v6
	v_med3_f32 v20, v53, s25, v6
	v_cvt_pk_fp8_f32 v14, v7, v20 op_sel:[0,0,1]
	v_med3_f32 v7, v65, s25, v6
	v_med3_f32 v20, v69, s25, v6
	v_cvt_pk_fp8_f32 v15, v7, v20 op_sel:[0,0,1]
	v_lshl_add_u64 v[24:25], s[4:5], 0, v[0:1]
	global_store_dwordx4 v0, v[8:11], s[4:5]
	global_store_dwordx4 v0, v[12:15], s[4:5] offset:2048
	v_med3_f32 v0, v88, s25, v6
	v_med3_f32 v7, v84, s25, v6
	v_mov_b32_e32 v8, v1
	v_cvt_pk_fp8_f32 v8, v0, v7
	v_med3_f32 v10, v22, s25, v6
	v_med3_f32 v11, v26, s25, v6
	v_mov_b32_e32 v9, v1
	v_cvt_pk_fp8_f32 v9, v10, v11
	v_med3_f32 v0, v18, s25, v6
	v_med3_f32 v7, v16, s25, v6
	v_cvt_pk_fp8_f32 v8, v0, v7 op_sel:[0,0,1]
	v_med3_f32 v0, v30, s25, v6
	v_med3_f32 v7, v34, s25, v6
	v_cvt_pk_fp8_f32 v9, v0, v7 op_sel:[0,0,1]
	v_med3_f32 v0, v38, s25, v6
	v_med3_f32 v7, v42, s25, v6
	v_mov_b32_e32 v10, v1
	v_cvt_pk_fp8_f32 v10, v0, v7
	v_med3_f32 v12, v54, s25, v6
	v_med3_f32 v13, v58, s25, v6
	v_mov_b32_e32 v11, v1
	v_cvt_pk_fp8_f32 v11, v12, v13
	v_pk_mul_f32 v[20:21], v[70:71], v[66:67] op_sel_hi:[1,0]
	v_med3_f32 v0, v46, s25, v6
	v_med3_f32 v7, v50, s25, v6
	v_cvt_pk_fp8_f32 v10, v0, v7 op_sel:[0,0,1]
	v_med3_f32 v0, v62, s25, v6
	v_med3_f32 v7, v20, s25, v6
	v_cvt_pk_fp8_f32 v11, v0, v7 op_sel:[0,0,1]
	v_med3_f32 v0, v89, s25, v6
	v_med3_f32 v7, v85, s25, v6
	v_mov_b32_e32 v12, v1
	v_cvt_pk_fp8_f32 v12, v0, v7
	v_med3_f32 v14, v23, s25, v6
	v_med3_f32 v15, v27, s25, v6
	v_mov_b32_e32 v13, v1
	v_cvt_pk_fp8_f32 v13, v14, v15
	v_med3_f32 v0, v19, s25, v6
	v_med3_f32 v7, v17, s25, v6
	v_cvt_pk_fp8_f32 v12, v0, v7 op_sel:[0,0,1]
	v_med3_f32 v0, v31, s25, v6
	v_med3_f32 v7, v35, s25, v6
	v_cvt_pk_fp8_f32 v13, v0, v7 op_sel:[0,0,1]
	v_med3_f32 v0, v39, s25, v6
	v_med3_f32 v7, v43, s25, v6
	v_mov_b32_e32 v14, v1
	v_cvt_pk_fp8_f32 v14, v0, v7
	v_med3_f32 v16, v55, s25, v6
	v_med3_f32 v17, v59, s25, v6
	v_mov_b32_e32 v15, v1
	v_cvt_pk_fp8_f32 v15, v16, v17
	v_med3_f32 v0, v47, s25, v6
	v_med3_f32 v7, v51, s25, v6
	v_cvt_pk_fp8_f32 v14, v0, v7 op_sel:[0,0,1]
	v_med3_f32 v0, v63, s25, v6
	v_med3_f32 v7, v21, s25, v6
	v_cvt_pk_fp8_f32 v15, v0, v7 op_sel:[0,0,1]
	v_add_co_u32_e32 v16, vcc, s26, v24
	s_add_i32 s4, s29, 1
	s_nop 0
	v_addc_co_u32_e32 v17, vcc, 0, v25, vcc
	v_mov_b32_e32 v0, s2
	v_mov_b32_e32 v7, s4
	global_store_dwordx4 v[16:17], v[8:11], off
	global_store_dwordx4 v[16:17], v[12:15], off offset:2048
	ds_write_b32 v0, v7

; __device__ __forceinline__ int lane_id_now() { unsigned z = 0u; asm volatile("" : "+v"(z)); return (int)__builtin_amdgcn_mbcnt_hi(~0u, __builtin_amdgcn_mbcnt_lo(~0u, z)); }
; #define GAS __attribute__((address_space(1)))
; template <bool GAIN, bool NT = false> __device__ __forceinline__ void titem8_load(const TItem& d, int lane, f32x4 (&r)[16], f32x4 (&g)[4]) {
;     const int q = lane & 7, kg = lane >> 3; const unsigned lo = (unsigned)((16 * kg) * d.N + 4 * q) * 4u;
;     const GAS char* base = (const GAS char*)d.src;
; #pragma unroll
;     for (int j = 0; j < 16; ++j) { const GAS f32x4* p = (const GAS f32x4*)(base + (size_t)j * (size_t)d.N * 4 + lo); r[j] = NT ? __builtin_nontemporal_load(p) : *p; }
;     if constexpr (GAIN) { const GAS char* gb = (const GAS char*)d.gain; const unsigned go = (unsigned)(16 * kg) * 4u;
; #pragma unroll
;         for (int j4 = 0; j4 < 4; ++j4) g[j4] = *(const GAS f32x4*)(gb + 16 * j4 + go); }
;     asm volatile("" ::: "memory"); __builtin_amdgcn_sched_barrier(0);
; }
; __device__ __forceinline__ bool cv_one(const CvWork& w) {
;     ...
;     TItem d; { int r = it; const int e = r / CV_I_UP; r -= e * CV_I_UP; const int nb_ = 2 * FF / 32, kb = r / nb_, nbi = r % nb_;
;         d.src = w.wup + (size_t)e * D * 2 * FF + (size_t)(128 * kb) * (2 * FF) + 32 * nbi; d.dst = (bf16*)(w.wup8 + (size_t)e * 2 * FF * D + (size_t)(32 * nbi) * D + 128 * kb);
;         d.gain = w.gain + 128 * kb; d.N = 2 * FF; d.ldk = D; }
;     const int lane = lane_id_now();
;     f32x4 r[16], g[4]; titem8_load<true, true>(d, lane, r, g); titem8_store<true, true>(d, lane, r, g);
.LBB0_379:
	s_and_b64 vcc, exec, s[6:7]
	s_cbranch_vccz .LBB0_381
	s_ashr_i32 s4, s29, 31
	s_lshr_b32 s4, s4, 21
	s_add_i32 s5, s29, s4
	s_ashr_i32 s4, s5, 11
	s_and_b32 s5, s5, 0xfffff800
	s_sub_i32 s5, s29, s5
	s_ashr_i32 s6, s5, 31
	s_lshr_b32 s6, s6, 25
	s_add_i32 s6, s5, s6
	s_and_b32 s6, s6, 0xffffff80
	s_sub_i32 s30, s5, s6
	s_ashr_i32 s5, s4, 31
	s_lshl_b64 s[8:9], s[4:5], 25
	s_add_u32 s31, s58, s8
	s_addc_u32 s33, s59, s9
	s_ashr_i32 s7, s6, 31
	v_mov_b32_e32 v0, 0
	s_lshl_b64 s[8:9], s[6:7], 14
	s_add_u32 s34, s31, s8
	v_mbcnt_lo_u32_b32 v0, -1, v0
	s_addc_u32 s33, s33, s9
	s_lshl_b32 s8, s30, 5
	v_mbcnt_hi_u32_b32 v0, -1, v0
	s_ashr_i32 s9, s8, 31
	v_lshlrev_b32_e32 v7, 1, v0
	v_lshlrev_b32_e32 v0, 2, v0
	s_lshl_b64 s[30:31], s[8:9], 2
	v_and_b32_e32 v88, 28, v0
	s_add_u32 s30, s34, s30
	v_and_b32_e32 v7, -16, v7
	v_lshlrev_b32_e32 v0, 2, v88
	s_addc_u32 s31, s33, s31
	v_lshl_or_b32 v0, v7, 14, v0
	v_lshl_add_u64 v[68:69], s[30:31], 0, v[0:1]
	v_add_co_u32_e32 v12, vcc, s11, v68
	s_lshl_b64 s[4:5], s[4:5], 23
	s_nop 0
	v_addc_co_u32_e32 v13, vcc, 0, v69, vcc
	v_add_co_u32_e32 v16, vcc, s12, v68
	s_add_u32 s33, s88, s4
	s_nop 0
	v_addc_co_u32_e32 v17, vcc, 0, v69, vcc
	v_add_co_u32_e32 v20, vcc, s13, v68
	s_addc_u32 s34, s87, s5
	s_nop 0
	v_addc_co_u32_e32 v21, vcc, 0, v69, vcc
	v_add_co_u32_e32 v24, vcc, s3, v68
	s_lshl_b64 s[4:5], s[8:9], 11
	s_nop 0
	v_addc_co_u32_e32 v25, vcc, 0, v69, vcc
	v_add_co_u32_e32 v28, vcc, s14, v68
	s_add_u32 s4, s33, s4
	s_nop 0
	v_addc_co_u32_e32 v29, vcc, 0, v69, vcc
	v_add_co_u32_e32 v32, vcc, s15, v68
	s_addc_u32 s5, s34, s5
	s_nop 0
	v_addc_co_u32_e32 v33, vcc, 0, v69, vcc
	v_add_co_u32_e32 v36, vcc, s16, v68
	s_add_u32 s4, s4, s6
	s_nop 0
	v_addc_co_u32_e32 v37, vcc, 0, v69, vcc
	v_add_co_u32_e32 v40, vcc, s17, v68
	s_addc_u32 s5, s5, s7
	s_nop 0
	v_addc_co_u32_e32 v41, vcc, 0, v69, vcc
	v_add_co_u32_e32 v44, vcc, s18, v68
	s_lshl_b64 s[6:7], s[6:7], 2
	s_nop 0
	v_addc_co_u32_e32 v45, vcc, 0, v69, vcc
	v_add_co_u32_e32 v48, vcc, s19, v68
	s_add_u32 s6, s52, s6
	s_nop 0
	v_addc_co_u32_e32 v49, vcc, 0, v69, vcc
	v_add_co_u32_e32 v52, vcc, s20, v68
	s_addc_u32 s7, s53, s7
	s_nop 0
	v_addc_co_u32_e32 v53, vcc, 0, v69, vcc
	v_add_co_u32_e32 v56, vcc, s21, v68
	global_load_dwordx4 v[8:11], v0, s[30:31] nt
	s_nop 0
	v_addc_co_u32_e32 v57, vcc, 0, v69, vcc
	v_add_co_u32_e32 v60, vcc, s22, v68
	v_lshlrev_b32_e32 v0, 2, v7
	s_nop 0
	v_addc_co_u32_e32 v61, vcc, 0, v69, vcc
	v_add_co_u32_e32 v64, vcc, s23, v68
	global_load_dwordx4 v[12:15], v[12:13], off nt
	s_nop 0
	global_load_dwordx4 v[16:19], v[16:17], off nt
	v_addc_co_u32_e32 v65, vcc, 0, v69, vcc
	v_add_co_u32_e32 v68, vcc, s24, v68
	global_load_dwordx4 v[20:23], v[20:21], off nt
	s_nop 0
	global_load_dwordx4 v[24:27], v[24:25], off nt
	v_addc_co_u32_e32 v69, vcc, 0, v69, vcc
	global_load_dwordx4 v[28:31], v[28:29], off nt
	s_nop 0
	global_load_dwordx4 v[32:35], v[32:33], off nt
	s_nop 0
	global_load_dwordx4 v[36:39], v[36:37], off nt
	s_nop 0
	global_load_dwordx4 v[40:43], v[40:41], off nt
	s_nop 0
	global_load_dwordx4 v[44:47], v[44:45], off nt
	s_nop 0
	global_load_dwordx4 v[48:51], v[48:49], off nt
	s_nop 0
	global_load_dwordx4 v[52:55], v[52:53], off nt
	s_nop 0
	global_load_dwordx4 v[56:59], v[56:57], off nt
	s_nop 0
	global_load_dwordx4 v[60:63], v[60:61], off nt
	s_nop 0
	global_load_dwordx4 v[64:67], v[64:65], off nt
	s_nop 0
	global_load_dwordx4 v[68:71], v[68:69], off nt
	s_nop 0
	global_load_dwordx4 v[72:75], v0, s[6:7] offset:48
	global_load_dwordx4 v[76:79], v0, s[6:7] offset:32
	global_load_dwordx4 v[80:83], v0, s[6:7] offset:16
	global_load_dwordx4 v[84:87], v0, s[6:7]
	s_waitcnt vmcnt(0)
; #define GAS __attribute__((address_space(1)))
; template <bool GAIN, bool NT = false> __device__ __forceinline__ void titem8_store(const TItem& d, int lane, const f32x4 (&r)[16], const f32x4 (&g)[4]) {
;     const int q = lane & 7, kg = lane >> 3; const unsigned lo = (unsigned)((4 * q) * d.ldk + 16 * kg);
;     GAS char* base = (GAS char*)d.dst;
;     f32x4 s[16];
; #pragma unroll
;     for (int j = 0; j < 16; ++j) s[j] = r[j] * ((GAIN ? g[j >> 2][j & 3] : 1.0f) * W8_SCALE);
; #pragma unroll
;     for (int i = 0; i < 4; ++i) { v4u w;
;         w.x = pk4_fp8w(s[0][i], s[1][i], s[2][i], s[3][i]); w.y = pk4_fp8w(s[4][i], s[5][i], s[6][i], s[7][i]);
;         w.z = pk4_fp8w(s[8][i], s[9][i], s[10][i], s[11][i]); w.w = pk4_fp8w(s[12][i], s[13][i], s[14][i], s[15][i]);
;         GAS v4u* p = (GAS v4u*)(base + (size_t)i * (size_t)d.ldk + lo);
;         if (NT) __builtin_nontemporal_store(w, p); else *p = w; }
; }
; __device__ __forceinline__ bool cv_one(const CvWork& w) {
;     ...
;     f32x4 r[16], g[4]; titem8_load<true, true>(d, lane, r, g); titem8_store<true, true>(d, lane, r, g);
;     w.cur[2 * w.wave] = it + 1;
	v_mul_f32_e32 v84, 0x43800000, v84
	v_pk_mul_f32 v[90:91], v[8:9], v[84:85] op_sel_hi:[1,0]
	v_mul_f32_e32 v8, 0x43800000, v85
	v_lshl_add_u32 v0, v88, 11, v7
	v_pk_mul_f32 v[88:89], v[10:11], v[84:85] op_sel_hi:[1,0]
	v_pk_mul_f32 v[84:85], v[14:15], v[8:9] op_sel_hi:[1,0]
	v_pk_mul_f32 v[12:13], v[12:13], v[8:9] op_sel_hi:[1,0]
	v_mul_f32_e32 v8, 0x43800000, v86
	v_pk_mul_f32 v[18:19], v[18:19], v[8:9] op_sel_hi:[1,0]
	v_pk_mul_f32 v[14:15], v[16:17], v[8:9] op_sel_hi:[1,0]
	v_mul_f32_e32 v8, 0x43800000, v87
	v_pk_mul_f32 v[16:17], v[22:23], v[8:9] op_sel_hi:[1,0]
	v_pk_mul_f32 v[20:21], v[20:21], v[8:9] op_sel_hi:[1,0]
	v_mul_f32_e32 v8, 0x43800000, v80
	v_pk_mul_f32 v[22:23], v[26:27], v[8:9] op_sel_hi:[1,0]
	v_pk_mul_f32 v[24:25], v[24:25], v[8:9] op_sel_hi:[1,0]
	v_mul_f32_e32 v8, 0x43800000, v81
	v_pk_mul_f32 v[26:27], v[30:31], v[8:9] op_sel_hi:[1,0]
	v_pk_mul_f32 v[28:29], v[28:29], v[8:9] op_sel_hi:[1,0]
	v_mul_f32_e32 v8, 0x43800000, v82
	v_pk_mul_f32 v[30:31], v[34:35], v[8:9] op_sel_hi:[1,0]
	v_pk_mul_f32 v[32:33], v[32:33], v[8:9] op_sel_hi:[1,0]
	v_mul_f32_e32 v8, 0x43800000, v83
	v_pk_mul_f32 v[34:35], v[38:39], v[8:9] op_sel_hi:[1,0]
	v_pk_mul_f32 v[36:37], v[36:37], v[8:9] op_sel_hi:[1,0]
	v_mul_f32_e32 v8, 0x43800000, v76
	v_pk_mul_f32 v[38:39], v[42:43], v[8:9] op_sel_hi:[1,0]
	v_pk_mul_f32 v[40:41], v[40:41], v[8:9] op_sel_hi:[1,0]
	v_mul_f32_e32 v8, 0x43800000, v77
	v_pk_mul_f32 v[42:43], v[46:47], v[8:9] op_sel_hi:[1,0]
	v_pk_mul_f32 v[44:45], v[44:45], v[8:9] op_sel_hi:[1,0]
	v_mul_f32_e32 v8, 0x43800000, v78
	v_pk_mul_f32 v[46:47], v[50:51], v[8:9] op_sel_hi:[1,0]
	v_pk_mul_f32 v[48:49], v[48:49], v[8:9] op_sel_hi:[1,0]
	v_mul_f32_e32 v8, 0x43800000, v79
	v_pk_mul_f32 v[50:51], v[54:55], v[8:9] op_sel_hi:[1,0]
	v_pk_mul_f32 v[52:53], v[52:53], v[8:9] op_sel_hi:[1,0]
	v_mul_f32_e32 v8, 0x43800000, v72
	v_pk_mul_f32 v[54:55], v[58:59], v[8:9] op_sel_hi:[1,0]
	v_pk_mul_f32 v[56:57], v[56:57], v[8:9] op_sel_hi:[1,0]
	v_mul_f32_e32 v8, 0x43800000, v73
	v_pk_mul_f32 v[58:59], v[62:63], v[8:9] op_sel_hi:[1,0]
	v_pk_mul_f32 v[60:61], v[60:61], v[8:9] op_sel_hi:[1,0]
	v_mul_f32_e32 v8, 0x43800000, v74
	v_pk_mul_f32 v[62:63], v[66:67], v[8:9] op_sel_hi:[1,0]
	v_pk_mul_f32 v[64:65], v[64:65], v[8:9] op_sel_hi:[1,0]
	v_med3_f32 v7, v90, s25, v6
	v_med3_f32 v9, v12, s25, v6
	v_mov_b32_e32 v8, v1
	v_cvt_pk_fp8_f32 v8, v7, v9
	v_med3_f32 v11, v24, s25, v6
	v_med3_f32 v12, v28, s25, v6
	v_mov_b32_e32 v9, v1
	v_cvt_pk_fp8_f32 v9, v11, v12
	v_med3_f32 v7, v14, s25, v6
	v_med3_f32 v10, v20, s25, v6
	v_cvt_pk_fp8_f32 v8, v7, v10 op_sel:[0,0,1]
	v_med3_f32 v7, v32, s25, v6
	v_med3_f32 v10, v36, s25, v6
	v_cvt_pk_fp8_f32 v9, v7, v10 op_sel:[0,0,1]
	v_med3_f32 v7, v40, s25, v6
	v_med3_f32 v11, v44, s25, v6
	v_mov_b32_e32 v10, v1
	v_cvt_pk_fp8_f32 v10, v7, v11
	v_med3_f32 v14, v56, s25, v6
	v_med3_f32 v20, v60, s25, v6
	v_mov_b32_e32 v11, v1
	v_cvt_pk_fp8_f32 v11, v14, v20
	v_mul_f32_e32 v66, 0x43800000, v75
	v_pk_mul_f32 v[68:69], v[68:69], v[66:67] op_sel_hi:[1,0]
	v_med3_f32 v7, v48, s25, v6
	v_med3_f32 v12, v52, s25, v6
	v_cvt_pk_fp8_f32 v10, v7, v12 op_sel:[0,0,1]
	v_med3_f32 v7, v64, s25, v6
	v_med3_f32 v12, v68, s25, v6
	v_cvt_pk_fp8_f32 v11, v7, v12 op_sel:[0,0,1]
	v_med3_f32 v7, v91, s25, v6
	v_med3_f32 v13, v13, s25, v6
	v_mov_b32_e32 v12, v1
	v_cvt_pk_fp8_f32 v12, v7, v13
	v_med3_f32 v7, v15, s25, v6
	v_med3_f32 v15, v25, s25, v6
	v_med3_f32 v20, v29, s25, v6
	v_mov_b32_e32 v13, v1
	v_cvt_pk_fp8_f32 v13, v15, v20
	v_med3_f32 v14, v21, s25, v6
	v_cvt_pk_fp8_f32 v12, v7, v14 op_sel:[0,0,1]
	v_med3_f32 v7, v33, s25, v6
	v_med3_f32 v14, v37, s25, v6
	v_cvt_pk_fp8_f32 v13, v7, v14 op_sel:[0,0,1]
	v_med3_f32 v7, v41, s25, v6
	v_med3_f32 v15, v45, s25, v6
	v_mov_b32_e32 v14, v1
	v_cvt_pk_fp8_f32 v14, v7, v15
	v_med3_f32 v21, v57, s25, v6
	v_med3_f32 v24, v61, s25, v6
	v_mov_b32_e32 v15, v1
	v_cvt_pk_fp8_f32 v15, v21, v24
	v_med3_f32 v7, v49, s25, v6
	v_med3_f32 v20, v53, s25, v6
	v_cvt_pk_fp8_f32 v14, v7, v20 op_sel:[0,0,1]
	v_med3_f32 v7, v65, s25, v6
	v_med3_f32 v20, v69, s25, v6
	v_cvt_pk_fp8_f32 v15, v7, v20 op_sel:[0,0,1]
	v_lshl_add_u64 v[24:25], s[4:5], 0, v[0:1]
	global_store_dwordx4 v0, v[8:11], s[4:5]
	global_store_dwordx4 v0, v[12:15], s[4:5] offset:2048
	v_med3_f32 v0, v88, s25, v6
	v_med3_f32 v7, v84, s25, v6
	v_mov_b32_e32 v8, v1
	v_cvt_pk_fp8_f32 v8, v0, v7
	v_med3_f32 v10, v22, s25, v6
	v_med3_f32 v11, v26, s25, v6
	v_mov_b32_e32 v9, v1
	v_cvt_pk_fp8_f32 v9, v10, v11
	v_med3_f32 v0, v18, s25, v6
	v_med3_f32 v7, v16, s25, v6
	v_cvt_pk_fp8_f32 v8, v0, v7 op_sel:[0,0,1]
	v_med3_f32 v0, v30, s25, v6
	v_med3_f32 v7, v34, s25, v6
	v_cvt_pk_fp8_f32 v9, v0, v7 op_sel:[0,0,1]
	v_med3_f32 v0, v38, s25, v6
	v_med3_f32 v7, v42, s25, v6
	v_mov_b32_e32 v10, v1
	v_cvt_pk_fp8_f32 v10, v0, v7
	v_med3_f32 v12, v54, s25, v6
	v_med3_f32 v13, v58, s25, v6
	v_mov_b32_e32 v11, v1
	v_cvt_pk_fp8_f32 v11, v12, v13
	v_pk_mul_f32 v[20:21], v[70:71], v[66:67] op_sel_hi:[1,0]
	v_med3_f32 v0, v46, s25, v6
	v_med3_f32 v7, v50, s25, v6
	v_cvt_pk_fp8_f32 v10, v0, v7 op_sel:[0,0,1]
	v_med3_f32 v0, v62, s25, v6
	v_med3_f32 v7, v20, s25, v6
	v_cvt_pk_fp8_f32 v11, v0, v7 op_sel:[0,0,1]
	v_med3_f32 v0, v89, s25, v6
	v_med3_f32 v7, v85, s25, v6
	v_mov_b32_e32 v12, v1
	v_cvt_pk_fp8_f32 v12, v0, v7
	v_med3_f32 v14, v23, s25, v6
	v_med3_f32 v15, v27, s25, v6
	v_mov_b32_e32 v13, v1
	v_cvt_pk_fp8_f32 v13, v14, v15
	v_med3_f32 v0, v19, s25, v6
	v_med3_f32 v7, v17, s25, v6
	v_cvt_pk_fp8_f32 v12, v0, v7 op_sel:[0,0,1]
	v_med3_f32 v0, v31, s25, v6
	v_med3_f32 v7, v35, s25, v6
	v_cvt_pk_fp8_f32 v13, v0, v7 op_sel:[0,0,1]
	v_med3_f32 v0, v39, s25, v6
	v_med3_f32 v7, v43, s25, v6
	v_mov_b32_e32 v14, v1
	v_cvt_pk_fp8_f32 v14, v0, v7
	v_med3_f32 v16, v55, s25, v6
	v_med3_f32 v17, v59, s25, v6
	v_mov_b32_e32 v15, v1
	v_cvt_pk_fp8_f32 v15, v16, v17
	v_med3_f32 v0, v47, s25, v6
	v_med3_f32 v7, v51, s25, v6
	v_cvt_pk_fp8_f32 v14, v0, v7 op_sel:[0,0,1]
	v_med3_f32 v0, v63, s25, v6
	v_med3_f32 v7, v21, s25, v6
	v_cvt_pk_fp8_f32 v15, v0, v7 op_sel:[0,0,1]
	v_add_co_u32_e32 v16, vcc, s26, v24
	s_add_i32 s4, s29, 1
	s_nop 0
	v_addc_co_u32_e32 v17, vcc, 0, v25, vcc
	v_mov_b32_e32 v0, s2
	v_mov_b32_e32 v7, s4
	global_store_dwordx4 v[16:17], v[8:11], off
	global_store_dwordx4 v[16:17], v[12:15], off offset:2048
	ds_write_b32 v0, v7

; __device__ __forceinline__ int lane_id_now() { unsigned z = 0u; asm volatile("" : "+v"(z)); return (int)__builtin_amdgcn_mbcnt_hi(~0u, __builtin_amdgcn_mbcnt_lo(~0u, z)); }
; #define GAS __attribute__((address_space(1)))
; template <bool GAIN, bool NT = false> __device__ __forceinline__ void titem8_load(const TItem& d, int lane, f32x4 (&r)[16], f32x4 (&g)[4]) {
;     const int q = lane & 7, kg = lane >> 3; const unsigned lo = (unsigned)((16 * kg) * d.N + 4 * q) * 4u;
;     const GAS char* base = (const GAS char*)d.src;
; #pragma unroll
;     for (int j = 0; j < 16; ++j) { const GAS f32x4* p = (const GAS f32x4*)(base + (size_t)j * (size_t)d.N * 4 + lo); r[j] = NT ? __builtin_nontemporal_load(p) : *p; }
;     if constexpr (GAIN) { const GAS char* gb = (const GAS char*)d.gain; const unsigned go = (unsigned)(16 * kg) * 4u;
; #pragma unroll
;         for (int j4 = 0; j4 < 4; ++j4) g[j4] = *(const GAS f32x4*)(gb + 16 * j4 + go); }
;     asm volatile("" ::: "memory"); __builtin_amdgcn_sched_barrier(0);
; }
; __device__ __forceinline__ bool cv_one(const CvWork& w) {
;     ...
;     TItem d; { int r = it; const int e = r / CV_I_UP; r -= e * CV_I_UP; const int nb_ = 2 * FF / 32, kb = r / nb_, nbi = r % nb_;
;         d.src = w.wup + (size_t)e * D * 2 * FF + (size_t)(128 * kb) * (2 * FF) + 32 * nbi; d.dst = (bf16*)(w.wup8 + (size_t)e * 2 * FF * D + (size_t)(32 * nbi) * D + 128 * kb);
;         d.gain = w.gain + 128 * kb; d.N = 2 * FF; d.ldk = D; }
;     const int lane = lane_id_now();
;     f32x4 r[16], g[4]; titem8_load<true, true>(d, lane, r, g); titem8_store<true, true>(d, lane, r, g);
.LBB0_1428:
	s_and_b64 vcc, exec, s[6:7]
	s_cbranch_vccz .LBB0_1415
	s_ashr_i32 s4, s28, 31
	s_lshr_b32 s4, s4, 21
	s_add_i32 s5, s28, s4
	s_ashr_i32 s4, s5, 11
	s_and_b32 s5, s5, 0xfffff800
	s_sub_i32 s5, s28, s5
	s_ashr_i32 s6, s5, 31
	s_lshr_b32 s6, s6, 25
	s_add_i32 s6, s5, s6
	s_and_b32 s6, s6, 0xffffff80
	s_sub_i32 s10, s5, s6
	s_ashr_i32 s5, s4, 31
	s_lshl_b64 s[8:9], s[4:5], 25
	s_add_u32 s11, s58, s8
	s_addc_u32 s29, s59, s9
	s_ashr_i32 s7, s6, 31
	v_mov_b32_e32 v0, 0
	s_lshl_b64 s[8:9], s[6:7], 14
	s_add_u32 s30, s11, s8
	v_mbcnt_lo_u32_b32 v0, -1, v0
	s_addc_u32 s29, s29, s9
	s_lshl_b32 s8, s10, 5
	v_mbcnt_hi_u32_b32 v0, -1, v0
	s_ashr_i32 s9, s8, 31
	v_lshlrev_b32_e32 v5, 1, v0
	v_lshlrev_b32_e32 v0, 2, v0
	s_lshl_b64 s[10:11], s[8:9], 2
	v_and_b32_e32 v86, 28, v0
	s_add_u32 s10, s30, s10
	v_and_b32_e32 v5, -16, v5
	v_lshlrev_b32_e32 v0, 2, v86
	s_addc_u32 s11, s29, s11
	v_lshl_or_b32 v0, v5, 14, v0
	v_lshl_add_u64 v[66:67], s[10:11], 0, v[0:1]
	v_add_co_u32_e32 v10, vcc, s12, v66
	s_lshl_b64 s[4:5], s[4:5], 23
	s_nop 0
	v_addc_co_u32_e32 v11, vcc, 0, v67, vcc
	v_add_co_u32_e32 v14, vcc, s13, v66
	s_add_u32 s29, s88, s4
	s_nop 0
	v_addc_co_u32_e32 v15, vcc, 0, v67, vcc
	v_add_co_u32_e32 v18, vcc, s14, v66
	s_addc_u32 s30, s87, s5
	s_nop 0
	v_addc_co_u32_e32 v19, vcc, 0, v67, vcc
	v_add_co_u32_e32 v22, vcc, s2, v66
	s_lshl_b64 s[4:5], s[8:9], 11
	s_nop 0
	v_addc_co_u32_e32 v23, vcc, 0, v67, vcc
	v_add_co_u32_e32 v26, vcc, s15, v66
	s_add_u32 s4, s29, s4
	s_nop 0
	v_addc_co_u32_e32 v27, vcc, 0, v67, vcc
	v_add_co_u32_e32 v30, vcc, s16, v66
	s_addc_u32 s5, s30, s5
	s_nop 0
	v_addc_co_u32_e32 v31, vcc, 0, v67, vcc
	v_add_co_u32_e32 v34, vcc, s17, v66
	s_add_u32 s4, s4, s6
	s_nop 0
	v_addc_co_u32_e32 v35, vcc, 0, v67, vcc
	v_add_co_u32_e32 v38, vcc, s18, v66
	s_addc_u32 s5, s5, s7
	s_nop 0
	v_addc_co_u32_e32 v39, vcc, 0, v67, vcc
	v_add_co_u32_e32 v42, vcc, s19, v66
	s_lshl_b64 s[6:7], s[6:7], 2
	s_nop 0
	v_addc_co_u32_e32 v43, vcc, 0, v67, vcc
	v_add_co_u32_e32 v46, vcc, s20, v66
	s_add_u32 s6, s52, s6
	s_nop 0
	v_addc_co_u32_e32 v47, vcc, 0, v67, vcc
	v_add_co_u32_e32 v50, vcc, s21, v66
	s_addc_u32 s7, s53, s7
	s_nop 0
	v_addc_co_u32_e32 v51, vcc, 0, v67, vcc
	v_add_co_u32_e32 v54, vcc, s22, v66
	global_load_dwordx4 v[6:9], v0, s[10:11] nt
	s_nop 0
	v_addc_co_u32_e32 v55, vcc, 0, v67, vcc
	v_add_co_u32_e32 v58, vcc, s23, v66
	v_lshlrev_b32_e32 v0, 2, v5
	s_nop 0
	v_addc_co_u32_e32 v59, vcc, 0, v67, vcc
	v_add_co_u32_e32 v62, vcc, s24, v66
	global_load_dwordx4 v[10:13], v[10:11], off nt
	s_nop 0
	global_load_dwordx4 v[14:17], v[14:15], off nt
	v_addc_co_u32_e32 v63, vcc, 0, v67, vcc
	v_add_co_u32_e32 v66, vcc, s25, v66
	global_load_dwordx4 v[18:21], v[18:19], off nt
	s_nop 0
	global_load_dwordx4 v[22:25], v[22:23], off nt
	v_addc_co_u32_e32 v67, vcc, 0, v67, vcc
	global_load_dwordx4 v[26:29], v[26:27], off nt
	s_nop 0
	global_load_dwordx4 v[30:33], v[30:31], off nt
	s_nop 0
	global_load_dwordx4 v[34:37], v[34:35], off nt
	s_nop 0
	global_load_dwordx4 v[38:41], v[38:39], off nt
	s_nop 0
	global_load_dwordx4 v[42:45], v[42:43], off nt
	s_nop 0
	global_load_dwordx4 v[46:49], v[46:47], off nt
	s_nop 0
	global_load_dwordx4 v[50:53], v[50:51], off nt
	s_nop 0
	global_load_dwordx4 v[54:57], v[54:55], off nt
	s_nop 0
	global_load_dwordx4 v[58:61], v[58:59], off nt
	s_nop 0
	global_load_dwordx4 v[62:65], v[62:63], off nt
	s_nop 0
	global_load_dwordx4 v[66:69], v[66:67], off nt
	s_nop 0
	global_load_dwordx4 v[70:73], v0, s[6:7] offset:48
	global_load_dwordx4 v[74:77], v0, s[6:7] offset:32
	global_load_dwordx4 v[78:81], v0, s[6:7] offset:16
	global_load_dwordx4 v[82:85], v0, s[6:7]
	s_waitcnt vmcnt(0)
; #define GAS __attribute__((address_space(1)))
; template <bool GAIN, bool NT = false> __device__ __forceinline__ void titem8_store(const TItem& d, int lane, const f32x4 (&r)[16], const f32x4 (&g)[4]) {
;     const int q = lane & 7, kg = lane >> 3; const unsigned lo = (unsigned)((4 * q) * d.ldk + 16 * kg);
;     GAS char* base = (GAS char*)d.dst;
;     f32x4 s[16];
; #pragma unroll
;     for (int j = 0; j < 16; ++j) s[j] = r[j] * ((GAIN ? g[j >> 2][j & 3] : 1.0f) * W8_SCALE);
; #pragma unroll
;     for (int i = 0; i < 4; ++i) { v4u w;
;         w.x = pk4_fp8w(s[0][i], s[1][i], s[2][i], s[3][i]); w.y = pk4_fp8w(s[4][i], s[5][i], s[6][i], s[7][i]);
;         w.z = pk4_fp8w(s[8][i], s[9][i], s[10][i], s[11][i]); w.w = pk4_fp8w(s[12][i], s[13][i], s[14][i], s[15][i]);
;         GAS v4u* p = (GAS v4u*)(base + (size_t)i * (size_t)d.ldk + lo);
;         if (NT) __builtin_nontemporal_store(w, p); else *p = w; }
; }
; __device__ __forceinline__ bool cv_one(const CvWork& w) {
;     ...
;     f32x4 r[16], g[4]; titem8_load<true, true>(d, lane, r, g); titem8_store<true, true>(d, lane, r, g);
;     w.cur[2 * w.wave] = it + 1;
	v_mul_f32_e32 v82, 0x43800000, v82
	v_pk_mul_f32 v[88:89], v[6:7], v[82:83] op_sel_hi:[1,0]
	v_mul_f32_e32 v6, 0x43800000, v83
	v_lshl_add_u32 v0, v86, 11, v5
	v_pk_mul_f32 v[86:87], v[8:9], v[82:83] op_sel_hi:[1,0]
	v_pk_mul_f32 v[82:83], v[12:13], v[6:7] op_sel_hi:[1,0]
	v_pk_mul_f32 v[10:11], v[10:11], v[6:7] op_sel_hi:[1,0]
	v_mul_f32_e32 v6, 0x43800000, v84
	v_pk_mul_f32 v[16:17], v[16:17], v[6:7] op_sel_hi:[1,0]
	v_pk_mul_f32 v[12:13], v[14:15], v[6:7] op_sel_hi:[1,0]
	v_mul_f32_e32 v6, 0x43800000, v85
	v_pk_mul_f32 v[14:15], v[20:21], v[6:7] op_sel_hi:[1,0]
	v_pk_mul_f32 v[18:19], v[18:19], v[6:7] op_sel_hi:[1,0]
	v_mul_f32_e32 v6, 0x43800000, v78
	v_pk_mul_f32 v[20:21], v[24:25], v[6:7] op_sel_hi:[1,0]
	v_pk_mul_f32 v[22:23], v[22:23], v[6:7] op_sel_hi:[1,0]
	v_mul_f32_e32 v6, 0x43800000, v79
	v_pk_mul_f32 v[24:25], v[28:29], v[6:7] op_sel_hi:[1,0]
	v_pk_mul_f32 v[26:27], v[26:27], v[6:7] op_sel_hi:[1,0]
	v_mul_f32_e32 v6, 0x43800000, v80
	v_pk_mul_f32 v[28:29], v[32:33], v[6:7] op_sel_hi:[1,0]
	v_pk_mul_f32 v[30:31], v[30:31], v[6:7] op_sel_hi:[1,0]
	v_mul_f32_e32 v6, 0x43800000, v81
	v_pk_mul_f32 v[32:33], v[36:37], v[6:7] op_sel_hi:[1,0]
	v_pk_mul_f32 v[34:35], v[34:35], v[6:7] op_sel_hi:[1,0]
	v_mul_f32_e32 v6, 0x43800000, v74
	v_pk_mul_f32 v[36:37], v[40:41], v[6:7] op_sel_hi:[1,0]
	v_pk_mul_f32 v[38:39], v[38:39], v[6:7] op_sel_hi:[1,0]
	v_mul_f32_e32 v6, 0x43800000, v75
	v_pk_mul_f32 v[40:41], v[44:45], v[6:7] op_sel_hi:[1,0]
	v_pk_mul_f32 v[42:43], v[42:43], v[6:7] op_sel_hi:[1,0]
	v_mul_f32_e32 v6, 0x43800000, v76
	v_pk_mul_f32 v[44:45], v[48:49], v[6:7] op_sel_hi:[1,0]
	v_pk_mul_f32 v[46:47], v[46:47], v[6:7] op_sel_hi:[1,0]
	v_mul_f32_e32 v6, 0x43800000, v77
	v_pk_mul_f32 v[48:49], v[52:53], v[6:7] op_sel_hi:[1,0]
	v_pk_mul_f32 v[50:51], v[50:51], v[6:7] op_sel_hi:[1,0]
	v_mul_f32_e32 v6, 0x43800000, v70
	v_pk_mul_f32 v[52:53], v[56:57], v[6:7] op_sel_hi:[1,0]
	v_pk_mul_f32 v[54:55], v[54:55], v[6:7] op_sel_hi:[1,0]
	v_mul_f32_e32 v6, 0x43800000, v71
	v_pk_mul_f32 v[56:57], v[60:61], v[6:7] op_sel_hi:[1,0]
	v_pk_mul_f32 v[58:59], v[58:59], v[6:7] op_sel_hi:[1,0]
	v_mul_f32_e32 v6, 0x43800000, v72
	v_pk_mul_f32 v[60:61], v[64:65], v[6:7] op_sel_hi:[1,0]
	v_pk_mul_f32 v[62:63], v[62:63], v[6:7] op_sel_hi:[1,0]
	v_med3_f32 v5, v88, s26, v4
	v_med3_f32 v7, v10, s26, v4
	v_mov_b32_e32 v6, v1
	v_cvt_pk_fp8_f32 v6, v5, v7
	v_med3_f32 v9, v22, s26, v4
	v_med3_f32 v10, v26, s26, v4
	v_mov_b32_e32 v7, v1
	v_cvt_pk_fp8_f32 v7, v9, v10
	v_med3_f32 v5, v12, s26, v4
	v_med3_f32 v8, v18, s26, v4
	v_cvt_pk_fp8_f32 v6, v5, v8 op_sel:[0,0,1]
	v_med3_f32 v5, v30, s26, v4
	v_med3_f32 v8, v34, s26, v4
	v_cvt_pk_fp8_f32 v7, v5, v8 op_sel:[0,0,1]
	v_med3_f32 v5, v38, s26, v4
	v_med3_f32 v9, v42, s26, v4
	v_mov_b32_e32 v8, v1
	v_cvt_pk_fp8_f32 v8, v5, v9
	v_med3_f32 v12, v54, s26, v4
	v_med3_f32 v18, v58, s26, v4
	v_mov_b32_e32 v9, v1
	v_cvt_pk_fp8_f32 v9, v12, v18
	v_mul_f32_e32 v64, 0x43800000, v73
	v_pk_mul_f32 v[66:67], v[66:67], v[64:65] op_sel_hi:[1,0]
	v_med3_f32 v5, v46, s26, v4
	v_med3_f32 v10, v50, s26, v4
	v_cvt_pk_fp8_f32 v8, v5, v10 op_sel:[0,0,1]
	v_med3_f32 v5, v62, s26, v4
	v_med3_f32 v10, v66, s26, v4
	v_cvt_pk_fp8_f32 v9, v5, v10 op_sel:[0,0,1]
	v_med3_f32 v5, v89, s26, v4
	v_med3_f32 v11, v11, s26, v4
	v_mov_b32_e32 v10, v1
	v_cvt_pk_fp8_f32 v10, v5, v11
	v_med3_f32 v5, v13, s26, v4
	v_med3_f32 v13, v23, s26, v4
	v_med3_f32 v18, v27, s26, v4
	v_mov_b32_e32 v11, v1
	v_cvt_pk_fp8_f32 v11, v13, v18
	v_med3_f32 v12, v19, s26, v4
	v_cvt_pk_fp8_f32 v10, v5, v12 op_sel:[0,0,1]
	v_med3_f32 v5, v31, s26, v4
	v_med3_f32 v12, v35, s26, v4
	v_cvt_pk_fp8_f32 v11, v5, v12 op_sel:[0,0,1]
	v_med3_f32 v5, v39, s26, v4
	v_med3_f32 v13, v43, s26, v4
	v_mov_b32_e32 v12, v1
	v_cvt_pk_fp8_f32 v12, v5, v13
	v_med3_f32 v19, v55, s26, v4
	v_med3_f32 v22, v59, s26, v4
	v_mov_b32_e32 v13, v1
	v_cvt_pk_fp8_f32 v13, v19, v22
	v_med3_f32 v5, v47, s26, v4
	v_med3_f32 v18, v51, s26, v4
	v_cvt_pk_fp8_f32 v12, v5, v18 op_sel:[0,0,1]
	v_med3_f32 v5, v63, s26, v4
	v_med3_f32 v18, v67, s26, v4
	v_cvt_pk_fp8_f32 v13, v5, v18 op_sel:[0,0,1]
	v_lshl_add_u64 v[22:23], s[4:5], 0, v[0:1]
	global_store_dwordx4 v0, v[6:9], s[4:5]
	global_store_dwordx4 v0, v[10:13], s[4:5] offset:2048
	v_med3_f32 v0, v86, s26, v4
	v_med3_f32 v5, v82, s26, v4
	v_mov_b32_e32 v6, v1
	v_cvt_pk_fp8_f32 v6, v0, v5
	v_med3_f32 v8, v20, s26, v4
	v_med3_f32 v9, v24, s26, v4
	v_mov_b32_e32 v7, v1
	v_cvt_pk_fp8_f32 v7, v8, v9
	v_med3_f32 v0, v16, s26, v4
	v_med3_f32 v5, v14, s26, v4
	v_cvt_pk_fp8_f32 v6, v0, v5 op_sel:[0,0,1]
	v_med3_f32 v0, v28, s26, v4
	v_med3_f32 v5, v32, s26, v4
	v_cvt_pk_fp8_f32 v7, v0, v5 op_sel:[0,0,1]
	v_med3_f32 v0, v36, s26, v4
	v_med3_f32 v5, v40, s26, v4
	v_mov_b32_e32 v8, v1
	v_cvt_pk_fp8_f32 v8, v0, v5
	v_med3_f32 v10, v52, s26, v4
	v_med3_f32 v11, v56, s26, v4
	v_mov_b32_e32 v9, v1
	v_cvt_pk_fp8_f32 v9, v10, v11
	v_pk_mul_f32 v[18:19], v[68:69], v[64:65] op_sel_hi:[1,0]
	v_med3_f32 v0, v44, s26, v4
	v_med3_f32 v5, v48, s26, v4
	v_cvt_pk_fp8_f32 v8, v0, v5 op_sel:[0,0,1]
	v_med3_f32 v0, v60, s26, v4
	v_med3_f32 v5, v18, s26, v4
	v_cvt_pk_fp8_f32 v9, v0, v5 op_sel:[0,0,1]
	v_med3_f32 v0, v87, s26, v4
	v_med3_f32 v5, v83, s26, v4
	v_mov_b32_e32 v10, v1
	v_cvt_pk_fp8_f32 v10, v0, v5
	v_med3_f32 v12, v21, s26, v4
	v_med3_f32 v13, v25, s26, v4
	v_mov_b32_e32 v11, v1
	v_cvt_pk_fp8_f32 v11, v12, v13
	v_med3_f32 v0, v17, s26, v4
	v_med3_f32 v5, v15, s26, v4
	v_cvt_pk_fp8_f32 v10, v0, v5 op_sel:[0,0,1]
	v_med3_f32 v0, v29, s26, v4
	v_med3_f32 v5, v33, s26, v4
	v_cvt_pk_fp8_f32 v11, v0, v5 op_sel:[0,0,1]
	v_med3_f32 v0, v37, s26, v4
	v_med3_f32 v5, v41, s26, v4
	v_mov_b32_e32 v12, v1
	v_cvt_pk_fp8_f32 v12, v0, v5
	v_med3_f32 v14, v53, s26, v4
	v_med3_f32 v15, v57, s26, v4
	v_mov_b32_e32 v13, v1
	v_cvt_pk_fp8_f32 v13, v14, v15
	v_med3_f32 v0, v45, s26, v4
	v_med3_f32 v5, v49, s26, v4
	v_cvt_pk_fp8_f32 v12, v0, v5 op_sel:[0,0,1]
	v_med3_f32 v0, v61, s26, v4
	v_med3_f32 v5, v19, s26, v4
	v_cvt_pk_fp8_f32 v13, v0, v5 op_sel:[0,0,1]
	v_add_co_u32_e32 v14, vcc, s27, v22
	s_add_i32 s4, s28, 1
	s_nop 0
	v_addc_co_u32_e32 v15, vcc, 0, v23, vcc
	v_mov_b32_e32 v0, s4
	s_mov_b64 s[4:5], 0
	global_store_dwordx4 v[14:15], v[6:9], off
	global_store_dwordx4 v[14:15], v[10:13], off offset:2048
	ds_write_b32 v2, v0
	s_branch .LBB0_1415
